# P9: the re-phased A half-tile pair issued after the load interval's ds_reads (all four LDS-DMA pieces behind the reads) instead of at its head
# baseline (speedup 1.0000x reference)
; #define PG8_STAGE(bufoff, gbase, voff) do { PG8_GLDS((const char*)(gbase), (voff)[0], ldsb + (bufoff)); PG8_GLDS((const char*)(gbase), (voff)[1], ldsb + (bufoff) + 8192u); } while (0)
; #define PG8_STAGEA(bufoff, gbase, o0, o1) do { PG8_GLDS((const char*)(gbase), (o0), ldsb + (bufoff)); PG8_GLDS((const char*)(gbase), (o1), ldsb + (bufoff) + 8192u); } while (0)
; template <class Epi, class Sched, bool F8 = false, bool PF = false, bool I8 = false, int PID = -1>
; __device__ __forceinline__ void gemm_phase(LAS unsigned char* lds, LAS unsigned char* xlds, const int RP, const int RPB, const int nt, const Sched& S, const Epi& E, const int stagger_ticks) {
;     ...
;             const char* a2 = last ? nA : cA + (size_t)(t + 2) * kstep; const char* b2 = last ? nB : cB + (size_t)(t + 2) * kstep;
;             const char* a3 = a2 + kstep; const char* b3 = b2 + kstep;
;             if constexpr (PF) { const char* pfa = (t + 4 < nt) ? cA + (size_t)(t + 4) * kstep : nA + (size_t)(t + 4 - nt) * kstep;
;                 asm volatile("s_mov_b32 m0, %2\n\ts_nop 0\n\tglobal_load_lds_dword %0, %1" :: "v"(voffP), "s"(pfa), "s"(ldsP) : "memory", "m0"); }
;             const bool relax = (Epi::RELAX > 0) && (t == 0) && epi_ran;
;             PG8_LDB(B0, 0, 0); PG8_LDB(B1, 0, 1); PG8_SCHED; PG8_LDA(At, 0, 0); PG8_STAGEA1(PG8_SA(1, 1), a1);
;             if (Sched::GATHER) { if (last) { const u32x4 nv = *nslot; vA0 = nv.x; vA1 = nv.y; vA2 = nv.z; vA3 = nv.w; } }
;             PG8_WAIT_VX(); PG8_WAIT_L(0); PG8_BAR; PG8_MMA(0, 0, At, B0); PG8_MMA(0, 1, At, B1); PG8_BAR; PG8_SCHED;
;             if constexpr (Epi::BIAS_DMA) { if (t == 0 && has_next) E.bias_dma(nxt, xlds + 8192 + ((ui + 1) & 1) * Epi::BIAS_STRIDE, wid, lane); }
;             PG8_LDA(At, 0, 1); PG8_STAGE(PG8_SB(0, 0), b2, voffB); PG8_STAGE(PG8_SB(0, 1), b2 + hstepB, voffB); PG8_STAGEA(PG8_SA(0, 0), a2, vA0, vA1);
;             PG8_WAIT_VX(); PG8_WAIT_L(0); PG8_BAR; PG8_MMA(1, 0, At, B0); PG8_MMA(1, 1, At, B1); PG8_BAR; PG8_SCHED;
;             PG8_LDB(B0, 1, 0); PG8_LDB(B1, 1, 1); PG8_SCHED; PG8_LDA(At, 1, 0); PG8_STAGEA1(PG8_SA(0, 1), a2);
;             PG8_WAIT_VR(); PG8_WAIT_L(0); PG8_BAR; PG8_MMA(0, 0, At, B0); PG8_MMA(0, 1, At, B1); PG8_BAR; PG8_SCHED;
;             PG8_LDA(At, 1, 1); PG8_STAGE(PG8_SB(1, 0), b3, voffB); PG8_STAGE(PG8_SB(1, 1), b3 + hstepB, voffB); PG8_STAGEA(PG8_SA(1, 0), a3, vA0, vA1);
.LBB0_1062:
	s_add_u32 s30, s26, 0xfffe0080
	s_addc_u32 s31, s27, -1
	s_cmp_eq_u32 s73, 4
	s_cselect_b32 s38, s6, s30
	s_cselect_b32 s39, s7, s31
	s_cselect_b32 s34, s8, s25
	s_cselect_b32 s35, s9, s71
	s_add_u32 s30, s38, 0x80
	s_addc_u32 s31, s39, 0
	s_add_u32 s36, s34, 0x80
	s_addc_u32 s37, s35, 0
	ds_read_b128 v[170:173], v169 offset:16384
	ds_read_b128 v[174:177], v169 offset:17408
	ds_read_b128 v[178:181], v169 offset:18432
	ds_read_b128 v[182:185], v169 offset:19456
	ds_read_b128 v[186:189], v169 offset:20480
	ds_read_b128 v[190:193], v169 offset:21504
	ds_read_b128 v[194:197], v169 offset:22528
	ds_read_b128 v[198:201], v169 offset:23552
	s_add_i32 s75, s74, 0x10000
	s_mov_b32 m0, s75
	s_nop 0
	global_load_lds_dwordx4 v166, s[34:35]
	s_add_i32 s75, s74, 0x12000
	s_mov_b32 m0, s75
	s_nop 0
	global_load_lds_dwordx4 v167, s[34:35]
	s_add_u32 s76, s34, 0x2000
	s_addc_u32 s77, s35, 0
	s_add_i32 s75, s74, 0x14000
	s_mov_b32 m0, s75
	s_nop 0
	global_load_lds_dwordx4 v166, s[76:77]
	s_add_i32 s75, s74, 0x16000
	s_mov_b32 m0, s75
	s_nop 0
	global_load_lds_dwordx4 v167, s[76:77]
	s_waitcnt vmcnt(6)
	s_waitcnt lgkmcnt(0)
	s_barrier
	s_setprio 1
	s_waitcnt lgkmcnt(6)
	v_mfma_f32_16x16x128_f8f6f4 v[86:89], v[2:9], v[170:177], v[86:89]
	v_mfma_f32_16x16x128_f8f6f4 v[82:85], v[10:17], v[170:177], v[82:85]
	s_waitcnt lgkmcnt(4)
	v_mfma_f32_16x16x128_f8f6f4 v[70:73], v[2:9], v[178:185], v[70:73]
	v_mfma_f32_16x16x128_f8f6f4 v[66:69], v[10:17], v[178:185], v[66:69]
	s_waitcnt lgkmcnt(2)
	v_mfma_f32_16x16x128_f8f6f4 v[202:205], v[2:9], v[186:193], v[54:57]
	v_mfma_f32_16x16x128_f8f6f4 v[206:209], v[10:17], v[186:193], v[50:53]
	s_waitcnt lgkmcnt(0)
	v_mfma_f32_16x16x128_f8f6f4 v[210:213], v[2:9], v[194:201], v[38:41]
	v_mfma_f32_16x16x128_f8f6f4 v[214:217], v[10:17], v[194:201], v[34:37]
	v_mfma_f32_16x16x128_f8f6f4 v[94:97], v[18:25], v[170:177], v[94:97]
	v_mfma_f32_16x16x128_f8f6f4 v[90:93], v[26:33], v[170:177], v[90:93]
	v_mfma_f32_16x16x128_f8f6f4 v[78:81], v[18:25], v[178:185], v[78:81]
	v_mfma_f32_16x16x128_f8f6f4 v[74:77], v[26:33], v[178:185], v[74:77]
	v_mfma_f32_16x16x128_f8f6f4 v[218:221], v[18:25], v[186:193], v[62:65]
	v_mfma_f32_16x16x128_f8f6f4 v[186:189], v[26:33], v[186:193], v[58:61]
	v_mfma_f32_16x16x128_f8f6f4 v[190:193], v[18:25], v[194:201], v[46:49]
	v_mfma_f32_16x16x128_f8f6f4 v[194:197], v[26:33], v[194:201], v[42:45]
	s_setprio 0
	s_barrier
	v_add_u32_e32 v14, 0x18000, v168
	v_add_u32_e32 v30, 0x1c000, v168
	ds_read_b128 v[2:5], v14
	ds_read_b128 v[6:9], v14 offset:1024
	ds_read_b128 v[10:13], v14 offset:2048
	ds_read_b128 v[14:17], v14 offset:3072
	ds_read_b128 v[18:21], v30
	ds_read_b128 v[22:25], v30 offset:1024
	ds_read_b128 v[26:29], v30 offset:2048
	ds_read_b128 v[30:33], v30 offset:3072
	ds_read_b128 v[34:37], v169 offset:32768
	ds_read_b128 v[38:41], v169 offset:33792
	ds_read_b128 v[42:45], v169 offset:34816
	ds_read_b128 v[46:49], v169 offset:35840
	ds_read_b128 v[50:53], v169 offset:36864
	ds_read_b128 v[54:57], v169 offset:37888
	ds_read_b128 v[58:61], v169 offset:38912
	ds_read_b128 v[62:65], v169 offset:39936
	s_add_i32 s75, s74, 0x2000
	s_mov_b32 m0, s74
	s_nop 0
	global_load_lds_dwordx4 v164, s[38:39]
	s_nop 0
	s_mov_b32 m0, s75
	s_nop 0
	global_load_lds_dwordx4 v165, s[38:39]
	s_add_u32 s38, s38, 0x20000
	s_addc_u32 s39, s39, 0
	s_add_i32 s75, s74, 0x4000
	s_mov_b32 m0, s75
	s_nop 0
	global_load_lds_dwordx4 v164, s[38:39]
	s_add_i32 s75, s74, 0x6000
	s_mov_b32 m0, s75
	s_nop 0
	global_load_lds_dwordx4 v165, s[38:39]
	s_waitcnt vmcnt(8)
	s_waitcnt lgkmcnt(0)
	s_barrier
	s_setprio 1
	s_waitcnt lgkmcnt(6)
	v_mfma_f32_16x16x128_f8f6f4 v[150:153], v[2:9], v[34:41], v[150:153]
	v_mfma_f32_16x16x128_f8f6f4 v[146:149], v[10:17], v[34:41], v[146:149]
	s_waitcnt lgkmcnt(4)
	v_mfma_f32_16x16x128_f8f6f4 v[134:137], v[2:9], v[42:49], v[134:137]
	v_mfma_f32_16x16x128_f8f6f4 v[130:133], v[10:17], v[42:49], v[130:133]
	s_waitcnt lgkmcnt(2)
	v_mfma_f32_16x16x128_f8f6f4 v[118:121], v[2:9], v[50:57], v[118:121]
	v_mfma_f32_16x16x128_f8f6f4 v[114:117], v[10:17], v[50:57], v[114:117]
	s_waitcnt lgkmcnt(0)
	v_mfma_f32_16x16x128_f8f6f4 v[102:105], v[2:9], v[58:65], v[102:105]
	v_mfma_f32_16x16x128_f8f6f4 v[98:101], v[10:17], v[58:65], v[98:101]
	v_mfma_f32_16x16x128_f8f6f4 v[158:161], v[18:25], v[34:41], v[158:161]
	v_mfma_f32_16x16x128_f8f6f4 v[154:157], v[26:33], v[34:41], v[154:157]
	v_mfma_f32_16x16x128_f8f6f4 v[142:145], v[18:25], v[42:49], v[142:145]
	v_mfma_f32_16x16x128_f8f6f4 v[138:141], v[26:33], v[42:49], v[138:141]
	v_mfma_f32_16x16x128_f8f6f4 v[126:129], v[18:25], v[50:57], v[126:129]
	v_mfma_f32_16x16x128_f8f6f4 v[122:125], v[26:33], v[50:57], v[122:125]
	v_mfma_f32_16x16x128_f8f6f4 v[110:113], v[18:25], v[58:65], v[110:113]
	v_mfma_f32_16x16x128_f8f6f4 v[106:109], v[26:33], v[58:65], v[106:109]
	s_setprio 0
	s_barrier
	ds_read_b128 v[42:45], v169 offset:49152
	ds_read_b128 v[46:49], v169 offset:50176
	ds_read_b128 v[58:61], v169 offset:51200
	ds_read_b128 v[62:65], v169 offset:52224
	ds_read_b128 v[170:173], v169 offset:53248
	ds_read_b128 v[174:177], v169 offset:54272
	ds_read_b128 v[178:181], v169 offset:55296
	ds_read_b128 v[182:185], v169 offset:56320
	s_add_i32 s38, s74, 0x18000
	s_mov_b32 m0, s38
	s_nop 0
	global_load_lds_dwordx4 v166, s[36:37]
	s_add_i32 s38, s74, 0x1a000
	s_mov_b32 m0, s38
	s_nop 0
	global_load_lds_dwordx4 v167, s[36:37]
	s_add_u32 s34, s34, 0x2080
	s_addc_u32 s35, s35, 0
	s_add_i32 s36, s74, 0x1c000
	s_mov_b32 m0, s36
	s_nop 0
	global_load_lds_dwordx4 v166, s[34:35]
	s_add_i32 s36, s74, 0x1e000
	s_mov_b32 m0, s36
	s_nop 0
	global_load_lds_dwordx4 v167, s[34:35]
	s_waitcnt vmcnt(6)
	s_waitcnt lgkmcnt(0)
	s_barrier
; #define PG8_STAGEA1(bufoff, gbase) do { if constexpr (Sched::GATHER) { PG8_STAGEA(bufoff, gbase, vA2, vA3); } else { PG8_STAGEA(bufoff, (gbase) + hstep, vA0, vA1); } } while (0)
; #define PG8_LDA(dst, b, h) do { if constexpr (F8) { _Pragma("unroll") for (int m = 0; m < 4; ++m) dst##8[m] = PG8_LD32(lds + PG8_SA(b, h) + aoff + m * 2048); } else { \
;         _Pragma("unroll") for (int m = 0; m < 4; ++m) _Pragma("unroll") for (int k = 0; k < 2; ++k) dst[m][k] = *(const LAS bf16x8*)(lds + PG8_SA(b, h) + aoff + m * 2048 + k * 1024); } } while (0)
; #define PG8_LDB(dst, b, h) do { if constexpr (F8) { _Pragma("unroll") for (int n = 0; n < 2; ++n) dst##8[n] = PG8_LD32(lds + PG8_SB(b, h) + boff + n * 2048); } else { \
;         _Pragma("unroll") for (int n = 0; n < 2; ++n) _Pragma("unroll") for (int k = 0; k < 2; ++k) dst[n][k] = *(const LAS bf16x8*)(lds + PG8_SB(b, h) + boff + n * 2048 + k * 1024); } } while (0)
; #define PG8_WAIT_VR() PG8_WAIT_V(8)
; #define PG8_WAIT_VX() do { if (relax) asm volatile("s_waitcnt vmcnt(%0)" :: "n"(8 + Epi::RELAX) : "memory"); else PG8_WAIT_V(8); } while (0)
; #define PG8_WAIT_L(n) asm volatile("s_waitcnt lgkmcnt(" #n ")" ::: "memory")
; #define PG8_BAR __builtin_amdgcn_s_barrier()
; #define PG8_SCHED __builtin_amdgcn_sched_barrier(0)
; template <class Epi, class Sched, bool F8 = false, bool PF = false, bool I8 = false, int PID = -1>
; __device__ __forceinline__ void gemm_phase(LAS unsigned char* lds, LAS unsigned char* xlds, const int RP, const int RPB, const int nt, const Sched& S, const Epi& E, const int stagger_ticks) {
;     ...
;             PG8_LDB(B0, 0, 0); PG8_LDB(B1, 0, 1); PG8_SCHED; PG8_LDA(At, 0, 0); PG8_STAGEA1(PG8_SA(1, 1), a1);
;             if (Sched::GATHER) { if (last) { const u32x4 nv = *nslot; vA0 = nv.x; vA1 = nv.y; vA2 = nv.z; vA3 = nv.w; } }
;             PG8_WAIT_VX(); PG8_WAIT_L(0); PG8_BAR; PG8_MMA(0, 0, At, B0); PG8_MMA(0, 1, At, B1); PG8_BAR; PG8_SCHED;
;             if constexpr (Epi::BIAS_DMA) { if (t == 0 && has_next) E.bias_dma(nxt, xlds + 8192 + ((ui + 1) & 1) * Epi::BIAS_STRIDE, wid, lane); }
;     ...
;             PG8_WAIT_VR(); PG8_WAIT_L(0); PG8_BAR; PG8_MMA(1, 0, At, B0); PG8_MMA(1, 1, At, B1); PG8_BAR; PG8_SCHED;
;         }
	s_setprio 1
	s_waitcnt lgkmcnt(6)
	v_mfma_f32_16x16x128_f8f6f4 v[86:89], v[2:9], v[42:49], v[86:89]
	v_mfma_f32_16x16x128_f8f6f4 v[82:85], v[10:17], v[42:49], v[82:85]
	s_waitcnt lgkmcnt(4)
	v_mfma_f32_16x16x128_f8f6f4 v[70:73], v[2:9], v[58:65], v[70:73]
	v_mfma_f32_16x16x128_f8f6f4 v[66:69], v[10:17], v[58:65], v[66:69]
	s_waitcnt lgkmcnt(2)
	v_mfma_f32_16x16x128_f8f6f4 v[54:57], v[2:9], v[170:177], v[202:205]
	v_mfma_f32_16x16x128_f8f6f4 v[50:53], v[10:17], v[170:177], v[206:209]
	s_waitcnt lgkmcnt(0)
	v_mfma_f32_16x16x128_f8f6f4 v[38:41], v[2:9], v[178:185], v[210:213]
	v_mfma_f32_16x16x128_f8f6f4 v[34:37], v[10:17], v[178:185], v[214:217]
	v_mfma_f32_16x16x128_f8f6f4 v[94:97], v[18:25], v[42:49], v[94:97]
	v_mfma_f32_16x16x128_f8f6f4 v[90:93], v[26:33], v[42:49], v[90:93]
	v_mfma_f32_16x16x128_f8f6f4 v[78:81], v[18:25], v[58:65], v[78:81]
	v_mfma_f32_16x16x128_f8f6f4 v[74:77], v[26:33], v[58:65], v[74:77]
	v_mfma_f32_16x16x128_f8f6f4 v[62:65], v[18:25], v[170:177], v[218:221]
	v_mfma_f32_16x16x128_f8f6f4 v[58:61], v[26:33], v[170:177], v[186:189]
	v_mfma_f32_16x16x128_f8f6f4 v[46:49], v[18:25], v[178:185], v[190:193]
	v_mfma_f32_16x16x128_f8f6f4 v[42:45], v[26:33], v[178:185], v[194:197]
	s_setprio 0
	s_barrier
	s_add_i32 s73, s73, 2
	s_add_u32 s25, s25, 0x100
	s_addc_u32 s71, s71, 0
	s_add_u32 s26, s26, 0x100
	s_addc_u32 s27, s27, 0
	s_cmp_gt_u32 s73, 5
	s_cbranch_scc1 .LBB0_1065
.LBB0_1063:
	s_mov_b32 s74, s47
	v_add_u32_e32 v14, 0x10000, v168
	v_add_u32_e32 v30, 0x14000, v168
	ds_read_b128 v[2:5], v14
	ds_read_b128 v[6:9], v14 offset:1024
	ds_read_b128 v[10:13], v14 offset:2048
	ds_read_b128 v[14:17], v14 offset:3072
	ds_read_b128 v[18:21], v30
	ds_read_b128 v[22:25], v30 offset:1024
	ds_read_b128 v[26:29], v30 offset:2048
	ds_read_b128 v[30:33], v30 offset:3072
	ds_read_b128 v[170:173], v169
	ds_read_b128 v[174:177], v169 offset:1024
	ds_read_b128 v[178:181], v169 offset:2048
	ds_read_b128 v[182:185], v169 offset:3072
	ds_read_b128 v[186:189], v169 offset:4096
	ds_read_b128 v[190:193], v169 offset:5120
	ds_read_b128 v[194:197], v169 offset:6144
	ds_read_b128 v[198:201], v169 offset:7168
	s_add_u32 s100, s26, 0xfffe0000
	s_addc_u32 s101, s27, -1
	s_add_i32 s30, s74, 0x8000
	s_mov_b32 m0, s30
	s_nop 0
	global_load_lds_dwordx4 v164, s[100:101]
	s_add_i32 s30, s74, 0xa000
	s_mov_b32 m0, s30
	s_nop 0
	global_load_lds_dwordx4 v165, s[100:101]
	s_add_i32 s30, s74, 0xc000
	s_mov_b32 m0, s30
	s_nop 0
	global_load_lds_dwordx4 v164, s[26:27]
	s_add_i32 s30, s74, 0xe000
	s_mov_b32 m0, s30
	s_nop 0
	global_load_lds_dwordx4 v165, s[26:27]
	s_waitcnt vmcnt(8)
	s_waitcnt lgkmcnt(0)
	s_barrier
	s_setprio 1
	s_waitcnt lgkmcnt(6)
	v_mfma_f32_16x16x128_f8f6f4 v[150:153], v[2:9], v[170:177], v[150:153]
	v_mfma_f32_16x16x128_f8f6f4 v[146:149], v[10:17], v[170:177], v[146:149]
	s_waitcnt lgkmcnt(4)
	v_mfma_f32_16x16x128_f8f6f4 v[134:137], v[2:9], v[178:185], v[134:137]
	v_mfma_f32_16x16x128_f8f6f4 v[130:133], v[10:17], v[178:185], v[130:133]
	s_waitcnt lgkmcnt(2)
	v_mfma_f32_16x16x128_f8f6f4 v[118:121], v[2:9], v[186:193], v[118:121]
	v_mfma_f32_16x16x128_f8f6f4 v[114:117], v[10:17], v[186:193], v[114:117]
	s_waitcnt lgkmcnt(0)
	v_mfma_f32_16x16x128_f8f6f4 v[102:105], v[2:9], v[194:201], v[102:105]
	v_mfma_f32_16x16x128_f8f6f4 v[98:101], v[10:17], v[194:201], v[98:101]
	v_mfma_f32_16x16x128_f8f6f4 v[158:161], v[18:25], v[170:177], v[158:161]
	v_mfma_f32_16x16x128_f8f6f4 v[154:157], v[26:33], v[170:177], v[154:157]
	v_mfma_f32_16x16x128_f8f6f4 v[142:145], v[18:25], v[178:185], v[142:145]
	v_mfma_f32_16x16x128_f8f6f4 v[138:141], v[26:33], v[178:185], v[138:141]
	v_mfma_f32_16x16x128_f8f6f4 v[126:129], v[18:25], v[186:193], v[126:129]
	v_mfma_f32_16x16x128_f8f6f4 v[122:125], v[26:33], v[186:193], v[122:125]
	v_mfma_f32_16x16x128_f8f6f4 v[110:113], v[18:25], v[194:201], v[110:113]
	v_mfma_f32_16x16x128_f8f6f4 v[106:109], v[26:33], v[194:201], v[106:109]
	s_setprio 0
	s_barrier
	s_cmp_lg_u32 s73, -2
	s_cselect_b64 s[30:31], -1, 0
	s_or_b64 s[30:31], s[30:31], s[28:29]
	s_and_b64 vcc, exec, s[30:31]
	s_cbranch_vccnz .LBB0_1062
	s_mov_b32 m0, s72
	s_nop 0
	global_load_lds_dword v1, s[2:3]
	s_branch .LBB0_1062
.Lmy_z8t:
	s_mov_b32 s74, s47
	v_add_u32_e32 v14, 0x10000, v168
	v_add_u32_e32 v30, 0x14000, v168
	ds_read_b128 v[2:5], v14
	ds_read_b128 v[6:9], v14 offset:1024
	ds_read_b128 v[10:13], v14 offset:2048
	ds_read_b128 v[14:17], v14 offset:3072
	ds_read_b128 v[18:21], v30
	ds_read_b128 v[22:25], v30 offset:1024
	ds_read_b128 v[26:29], v30 offset:2048
	ds_read_b128 v[30:33], v30 offset:3072
	ds_read_b128 v[170:173], v169
	ds_read_b128 v[174:177], v169 offset:1024
	ds_read_b128 v[178:181], v169 offset:2048
	ds_read_b128 v[182:185], v169 offset:3072
	ds_read_b128 v[186:189], v169 offset:4096
	ds_read_b128 v[190:193], v169 offset:5120
	ds_read_b128 v[194:197], v169 offset:6144
	ds_read_b128 v[198:201], v169 offset:7168
	s_add_u32 s100, s26, 0xfffe0000
	s_addc_u32 s101, s27, -1
	s_add_i32 s30, s74, 0x8000
	s_mov_b32 m0, s30
	s_nop 0
	global_load_lds_dwordx4 v164, s[100:101]
	s_add_i32 s30, s74, 0xa000
	s_mov_b32 m0, s30
	s_nop 0
	global_load_lds_dwordx4 v165, s[100:101]
	s_add_i32 s30, s74, 0xc000
	s_mov_b32 m0, s30
	s_nop 0
	global_load_lds_dwordx4 v164, s[26:27]
	s_add_i32 s30, s74, 0xe000
	s_mov_b32 m0, s30
	s_nop 0
	global_load_lds_dwordx4 v165, s[26:27]
	s_waitcnt vmcnt(8)
	s_waitcnt lgkmcnt(0)
	s_barrier
	s_setprio 1
	s_waitcnt lgkmcnt(6)
	v_mfma_f32_16x16x128_f8f6f4 v[150:153], v[2:9], v[170:177], 0
	v_mfma_f32_16x16x128_f8f6f4 v[146:149], v[10:17], v[170:177], 0
	s_waitcnt lgkmcnt(4)
	v_mfma_f32_16x16x128_f8f6f4 v[134:137], v[2:9], v[178:185], 0
	v_mfma_f32_16x16x128_f8f6f4 v[130:133], v[10:17], v[178:185], 0
	s_waitcnt lgkmcnt(2)
	v_mfma_f32_16x16x128_f8f6f4 v[118:121], v[2:9], v[186:193], 0
	v_mfma_f32_16x16x128_f8f6f4 v[114:117], v[10:17], v[186:193], 0
	s_waitcnt lgkmcnt(0)
	v_mfma_f32_16x16x128_f8f6f4 v[102:105], v[2:9], v[194:201], 0
	v_mfma_f32_16x16x128_f8f6f4 v[98:101], v[10:17], v[194:201], 0
	v_mfma_f32_16x16x128_f8f6f4 v[158:161], v[18:25], v[170:177], 0
	v_mfma_f32_16x16x128_f8f6f4 v[154:157], v[26:33], v[170:177], 0
	v_mfma_f32_16x16x128_f8f6f4 v[142:145], v[18:25], v[178:185], 0
	v_mfma_f32_16x16x128_f8f6f4 v[138:141], v[26:33], v[178:185], 0
	v_mfma_f32_16x16x128_f8f6f4 v[126:129], v[18:25], v[186:193], 0
	v_mfma_f32_16x16x128_f8f6f4 v[122:125], v[26:33], v[186:193], 0
	v_mfma_f32_16x16x128_f8f6f4 v[110:113], v[18:25], v[194:201], 0
	v_mfma_f32_16x16x128_f8f6f4 v[106:109], v[26:33], v[194:201], 0
	s_setprio 0
	s_barrier
	s_cmp_lg_u32 s73, -2
	s_cselect_b64 s[30:31], -1, 0
	s_or_b64 s[30:31], s[30:31], s[28:29]
	s_and_b64 vcc, exec, s[30:31]
	s_cbranch_vccnz .Lmy_z8b
	s_mov_b32 m0, s72
	s_nop 0
	global_load_lds_dword v1, s[2:3]
	s_branch .Lmy_z8b
; #define PG8_STAGE(bufoff, gbase, voff) do { PG8_GLDS((const char*)(gbase), (voff)[0], ldsb + (bufoff)); PG8_GLDS((const char*)(gbase), (voff)[1], ldsb + (bufoff) + 8192u); } while (0)
; #define PG8_STAGEA(bufoff, gbase, o0, o1) do { PG8_GLDS((const char*)(gbase), (o0), ldsb + (bufoff)); PG8_GLDS((const char*)(gbase), (o1), ldsb + (bufoff) + 8192u); } while (0)
; #define PG8_STAGEA1(bufoff, gbase) do { if constexpr (Sched::GATHER) { PG8_STAGEA(bufoff, gbase, vA2, vA3); } else { PG8_STAGEA(bufoff, (gbase) + hstep, vA0, vA1); } } while (0)
; #define PG8_LDA(dst, b, h) do { if constexpr (F8) { _Pragma("unroll") for (int m = 0; m < 4; ++m) dst##8[m] = PG8_LD32(lds + PG8_SA(b, h) + aoff + m * 2048); } else { \
;         _Pragma("unroll") for (int m = 0; m < 4; ++m) _Pragma("unroll") for (int k = 0; k < 2; ++k) dst[m][k] = *(const LAS bf16x8*)(lds + PG8_SA(b, h) + aoff + m * 2048 + k * 1024); } } while (0)
; #define PG8_LDB(dst, b, h) do { if constexpr (F8) { _Pragma("unroll") for (int n = 0; n < 2; ++n) dst##8[n] = PG8_LD32(lds + PG8_SB(b, h) + boff + n * 2048); } else { \
;         _Pragma("unroll") for (int n = 0; n < 2; ++n) _Pragma("unroll") for (int k = 0; k < 2; ++k) dst[n][k] = *(const LAS bf16x8*)(lds + PG8_SB(b, h) + boff + n * 2048 + k * 1024); } } while (0)
; #define PG8_WAIT_VR() PG8_WAIT_V(8)
; template <class Epi, class Sched, bool F8 = false, bool PF = false, bool I8 = false, int PID = -1>
; __device__ __forceinline__ void gemm_phase(LAS unsigned char* lds, LAS unsigned char* xlds, const int RP, const int RPB, const int nt, const Sched& S, const Epi& E, const int stagger_ticks) {
;     ...
;             PG8_LDA(At, 0, 1); PG8_STAGE(PG8_SB(0, 0), b2, voffB); PG8_STAGE(PG8_SB(0, 1), b2 + hstepB, voffB); PG8_STAGEA(PG8_SA(0, 0), a2, vA0, vA1);
;             PG8_WAIT_VX(); PG8_WAIT_L(0); PG8_BAR; PG8_MMA(1, 0, At, B0); PG8_MMA(1, 1, At, B1); PG8_BAR; PG8_SCHED;
;             PG8_LDB(B0, 1, 0); PG8_LDB(B1, 1, 1); PG8_SCHED; PG8_LDA(At, 1, 0); PG8_STAGEA1(PG8_SA(0, 1), a2);
;             PG8_WAIT_VR(); PG8_WAIT_L(0); PG8_BAR; PG8_MMA(0, 0, At, B0); PG8_MMA(0, 1, At, B1); PG8_BAR; PG8_SCHED;
;             PG8_LDA(At, 1, 1); PG8_STAGE(PG8_SB(1, 0), b3, voffB); PG8_STAGE(PG8_SB(1, 1), b3 + hstepB, voffB); PG8_STAGEA(PG8_SA(1, 0), a3, vA0, vA1);
;             PG8_WAIT_VR(); PG8_WAIT_L(0); PG8_BAR; PG8_MMA(1, 0, At, B0); PG8_MMA(1, 1, At, B1); PG8_BAR; PG8_SCHED;
.Lmy_z8b:
	s_add_u32 s30, s26, 0xfffe0080
	s_addc_u32 s31, s27, -1
	s_cmp_eq_u32 s73, 4
	s_cselect_b32 s38, s6, s30
	s_cselect_b32 s39, s7, s31
	s_cselect_b32 s34, s8, s25
	s_cselect_b32 s35, s9, s71
	s_add_u32 s30, s38, 0x80
	s_addc_u32 s31, s39, 0
	s_add_u32 s36, s34, 0x80
	s_addc_u32 s37, s35, 0
	ds_read_b128 v[170:173], v169 offset:16384
	ds_read_b128 v[174:177], v169 offset:17408
	ds_read_b128 v[178:181], v169 offset:18432
	ds_read_b128 v[182:185], v169 offset:19456
	ds_read_b128 v[186:189], v169 offset:20480
	ds_read_b128 v[190:193], v169 offset:21504
	ds_read_b128 v[194:197], v169 offset:22528
	ds_read_b128 v[198:201], v169 offset:23552
	s_add_i32 s75, s74, 0x10000
	s_mov_b32 m0, s75
	s_nop 0
	global_load_lds_dwordx4 v166, s[34:35]
	s_add_i32 s75, s74, 0x12000
	s_mov_b32 m0, s75
	s_nop 0
	global_load_lds_dwordx4 v167, s[34:35]
	s_add_u32 s76, s34, 0x2000
	s_addc_u32 s77, s35, 0
	s_add_i32 s75, s74, 0x14000
	s_mov_b32 m0, s75
	s_nop 0
	global_load_lds_dwordx4 v166, s[76:77]
	s_add_i32 s75, s74, 0x16000
	s_mov_b32 m0, s75
	s_nop 0
	global_load_lds_dwordx4 v167, s[76:77]
	s_waitcnt vmcnt(6)
	s_waitcnt lgkmcnt(0)
	s_barrier
	s_setprio 1
	s_waitcnt lgkmcnt(6)
	v_mfma_f32_16x16x128_f8f6f4 v[86:89], v[2:9], v[170:177], 0
	v_mfma_f32_16x16x128_f8f6f4 v[82:85], v[10:17], v[170:177], 0
	s_waitcnt lgkmcnt(4)
	v_mfma_f32_16x16x128_f8f6f4 v[70:73], v[2:9], v[178:185], 0
	v_mfma_f32_16x16x128_f8f6f4 v[66:69], v[10:17], v[178:185], 0
	s_waitcnt lgkmcnt(2)
	v_mfma_f32_16x16x128_f8f6f4 v[202:205], v[2:9], v[186:193], 0
	v_mfma_f32_16x16x128_f8f6f4 v[206:209], v[10:17], v[186:193], 0
	s_waitcnt lgkmcnt(0)
	v_mfma_f32_16x16x128_f8f6f4 v[210:213], v[2:9], v[194:201], 0
	v_mfma_f32_16x16x128_f8f6f4 v[214:217], v[10:17], v[194:201], 0
	v_mfma_f32_16x16x128_f8f6f4 v[94:97], v[18:25], v[170:177], 0
	v_mfma_f32_16x16x128_f8f6f4 v[90:93], v[26:33], v[170:177], 0
	v_mfma_f32_16x16x128_f8f6f4 v[78:81], v[18:25], v[178:185], 0
	v_mfma_f32_16x16x128_f8f6f4 v[74:77], v[26:33], v[178:185], 0
	v_mfma_f32_16x16x128_f8f6f4 v[218:221], v[18:25], v[186:193], 0
	v_mfma_f32_16x16x128_f8f6f4 v[186:189], v[26:33], v[186:193], 0
	v_mfma_f32_16x16x128_f8f6f4 v[190:193], v[18:25], v[194:201], 0
	v_mfma_f32_16x16x128_f8f6f4 v[194:197], v[26:33], v[194:201], 0
	s_setprio 0
	s_barrier
	v_add_u32_e32 v14, 0x18000, v168
	v_add_u32_e32 v30, 0x1c000, v168
	ds_read_b128 v[2:5], v14
	ds_read_b128 v[6:9], v14 offset:1024
	ds_read_b128 v[10:13], v14 offset:2048
	ds_read_b128 v[14:17], v14 offset:3072
	ds_read_b128 v[18:21], v30
	ds_read_b128 v[22:25], v30 offset:1024
	ds_read_b128 v[26:29], v30 offset:2048
	ds_read_b128 v[30:33], v30 offset:3072
	ds_read_b128 v[34:37], v169 offset:32768
	ds_read_b128 v[38:41], v169 offset:33792
	ds_read_b128 v[42:45], v169 offset:34816
	ds_read_b128 v[46:49], v169 offset:35840
	ds_read_b128 v[50:53], v169 offset:36864
	ds_read_b128 v[54:57], v169 offset:37888
	ds_read_b128 v[58:61], v169 offset:38912
	ds_read_b128 v[62:65], v169 offset:39936
	s_add_i32 s75, s74, 0x2000
	s_mov_b32 m0, s74
	s_nop 0
	global_load_lds_dwordx4 v164, s[38:39]
	s_nop 0
	s_mov_b32 m0, s75
	s_nop 0
	global_load_lds_dwordx4 v165, s[38:39]
	s_add_u32 s38, s38, 0x20000
	s_addc_u32 s39, s39, 0
	s_add_i32 s75, s74, 0x4000
	s_mov_b32 m0, s75
	s_nop 0
	global_load_lds_dwordx4 v164, s[38:39]
	s_add_i32 s75, s74, 0x6000
	s_mov_b32 m0, s75
	s_nop 0
	global_load_lds_dwordx4 v165, s[38:39]
	s_waitcnt vmcnt(8)
	s_waitcnt lgkmcnt(0)
	s_barrier
	s_setprio 1
	s_waitcnt lgkmcnt(6)
	v_mfma_f32_16x16x128_f8f6f4 v[150:153], v[2:9], v[34:41], v[150:153]
	v_mfma_f32_16x16x128_f8f6f4 v[146:149], v[10:17], v[34:41], v[146:149]
	s_waitcnt lgkmcnt(4)
	v_mfma_f32_16x16x128_f8f6f4 v[134:137], v[2:9], v[42:49], v[134:137]
	v_mfma_f32_16x16x128_f8f6f4 v[130:133], v[10:17], v[42:49], v[130:133]
	s_waitcnt lgkmcnt(2)
	v_mfma_f32_16x16x128_f8f6f4 v[118:121], v[2:9], v[50:57], v[118:121]
	v_mfma_f32_16x16x128_f8f6f4 v[114:117], v[10:17], v[50:57], v[114:117]
	s_waitcnt lgkmcnt(0)
	v_mfma_f32_16x16x128_f8f6f4 v[102:105], v[2:9], v[58:65], v[102:105]
	v_mfma_f32_16x16x128_f8f6f4 v[98:101], v[10:17], v[58:65], v[98:101]
	v_mfma_f32_16x16x128_f8f6f4 v[158:161], v[18:25], v[34:41], v[158:161]
	v_mfma_f32_16x16x128_f8f6f4 v[154:157], v[26:33], v[34:41], v[154:157]
	v_mfma_f32_16x16x128_f8f6f4 v[142:145], v[18:25], v[42:49], v[142:145]
	v_mfma_f32_16x16x128_f8f6f4 v[138:141], v[26:33], v[42:49], v[138:141]
	v_mfma_f32_16x16x128_f8f6f4 v[126:129], v[18:25], v[50:57], v[126:129]
	v_mfma_f32_16x16x128_f8f6f4 v[122:125], v[26:33], v[50:57], v[122:125]
	v_mfma_f32_16x16x128_f8f6f4 v[110:113], v[18:25], v[58:65], v[110:113]
	v_mfma_f32_16x16x128_f8f6f4 v[106:109], v[26:33], v[58:65], v[106:109]
	s_setprio 0
	s_barrier
	ds_read_b128 v[42:45], v169 offset:49152
	ds_read_b128 v[46:49], v169 offset:50176
	ds_read_b128 v[58:61], v169 offset:51200
	ds_read_b128 v[62:65], v169 offset:52224
	ds_read_b128 v[170:173], v169 offset:53248
	ds_read_b128 v[174:177], v169 offset:54272
	ds_read_b128 v[178:181], v169 offset:55296
	ds_read_b128 v[182:185], v169 offset:56320
	s_add_i32 s38, s74, 0x18000
	s_mov_b32 m0, s38
	s_nop 0
	global_load_lds_dwordx4 v166, s[36:37]
	s_add_i32 s38, s74, 0x1a000
	s_mov_b32 m0, s38
	s_nop 0
	global_load_lds_dwordx4 v167, s[36:37]
	s_add_u32 s34, s34, 0x2080
	s_addc_u32 s35, s35, 0
	s_add_i32 s36, s74, 0x1c000
	s_mov_b32 m0, s36
	s_nop 0
	global_load_lds_dwordx4 v166, s[34:35]
	s_add_i32 s36, s74, 0x1e000
	s_mov_b32 m0, s36
	s_nop 0
	global_load_lds_dwordx4 v167, s[34:35]
	s_waitcnt vmcnt(6)
	s_waitcnt lgkmcnt(0)
	s_barrier
	s_setprio 1
	s_waitcnt lgkmcnt(6)
	v_mfma_f32_16x16x128_f8f6f4 v[86:89], v[2:9], v[42:49], v[86:89]
	v_mfma_f32_16x16x128_f8f6f4 v[82:85], v[10:17], v[42:49], v[82:85]
	s_waitcnt lgkmcnt(4)
	v_mfma_f32_16x16x128_f8f6f4 v[70:73], v[2:9], v[58:65], v[70:73]
	v_mfma_f32_16x16x128_f8f6f4 v[66:69], v[10:17], v[58:65], v[66:69]
	s_waitcnt lgkmcnt(2)
	v_mfma_f32_16x16x128_f8f6f4 v[54:57], v[2:9], v[170:177], v[202:205]
	v_mfma_f32_16x16x128_f8f6f4 v[50:53], v[10:17], v[170:177], v[206:209]
	s_waitcnt lgkmcnt(0)
	v_mfma_f32_16x16x128_f8f6f4 v[38:41], v[2:9], v[178:185], v[210:213]
	v_mfma_f32_16x16x128_f8f6f4 v[34:37], v[10:17], v[178:185], v[214:217]
	v_mfma_f32_16x16x128_f8f6f4 v[94:97], v[18:25], v[42:49], v[94:97]
	v_mfma_f32_16x16x128_f8f6f4 v[90:93], v[26:33], v[42:49], v[90:93]
	v_mfma_f32_16x16x128_f8f6f4 v[78:81], v[18:25], v[58:65], v[78:81]
	v_mfma_f32_16x16x128_f8f6f4 v[74:77], v[26:33], v[58:65], v[74:77]
	v_mfma_f32_16x16x128_f8f6f4 v[62:65], v[18:25], v[170:177], v[218:221]
	v_mfma_f32_16x16x128_f8f6f4 v[58:61], v[26:33], v[170:177], v[186:189]
	v_mfma_f32_16x16x128_f8f6f4 v[46:49], v[18:25], v[178:185], v[190:193]
	v_mfma_f32_16x16x128_f8f6f4 v[42:45], v[26:33], v[178:185], v[194:197]
	s_setprio 0
	s_barrier
	s_add_i32 s73, s73, 2
	s_add_u32 s25, s25, 0x100
	s_addc_u32 s71, s71, 0
	s_add_u32 s26, s26, 0x100
	s_addc_u32 s27, s27, 0
	s_cmp_gt_u32 s73, 5
	s_branch .LBB0_1063
